# P0 expert weight conversion rewritten by hand: 4 register banks of 8 row loads per wave, each bank refilled with the next strip right after it is converted (24-32 loads always in flight), same math an
# baseline (speedup 1.0000x reference)
.LBB0_156:
	v_mov_b32_e32 v1, v0
	s_waitcnt lgkmcnt(0)
	s_barrier
	v_and_b32_e32 v1, 63, v0
	v_and_b32_e32 v2, 15, v1
	v_lshrrev_b32_e32 v3, 4, v1
	v_lshrrev_b32_e32 v4, 3, v1
	v_and_b32_e32 v5, 7, v1
	v_lshrrev_b32_e32 v20, 6, v0
	s_nop 0
	v_readfirstlane_b32 s8, v20
	s_lshl_b32 s9, s8, 13
	s_add_u32 s9, s9, 0x10000
	v_lshlrev_b32_e32 v20, 4, v2
	v_lshl_add_u32 v6, v3, 17, v20
	v_lshl_add_u32 v7, v3, 16, v20
	v_lshlrev_b32_e32 v21, 4, v5
	v_lshl_add_u32 v9, v4, 11, v21
	v_and_b32_e32 v22, 1, v4
	v_lshlrev_b32_e32 v22, 7, v22
	v_lshrrev_b32_e32 v23, 1, v4
	v_add_u32_e32 v22, v22, v23
	v_lshl_add_u32 v10, v22, 11, v21
	v_and_b32_e32 v22, 7, v2
	v_lshlrev_b32_e32 v22, 1, v22
	v_xor_b32_e32 v22, v22, v3
	v_lshlrev_b32_e32 v22, 3, v22
	v_lshlrev_b32_e32 v23, 9, v2
	v_add_u32_e32 v23, s9, v23
	v_xor_b32_e32 v12, 0, v22
	v_add_u32_e32 v12, v12, v23
	v_xor_b32_e32 v13, 32, v22
	v_add_u32_e32 v13, v13, v23
	v_xor_b32_e32 v14, 64, v22
	v_add_u32_e32 v14, v14, v23
	v_xor_b32_e32 v15, 96, v22
	v_add_u32_e32 v15, v15, v23
	v_lshrrev_b32_e32 v22, 2, v4
	v_lshlrev_b32_e32 v22, 4, v22
	v_xor_b32_e32 v22, v22, v21
	v_lshlrev_b32_e32 v23, 7, v4
	v_add_u32_e32 v23, s9, v23
	v_xor_b32_e32 v16, 0, v22
	v_add_u32_e32 v16, v16, v23
	v_xor_b32_e32 v17, 32, v22
	v_add_u32_e32 v17, v17, v23
	v_xor_b32_e32 v18, 64, v22
	v_add_u32_e32 v18, v18, v23
	v_xor_b32_e32 v19, 96, v22
	v_add_u32_e32 v19, v19, v23
	v_mov_b32_e32 v24, 0x42800000
	v_mov_b32_e32 v25, 0x42800000
	v_mov_b32_e32 v20, 0
	v_mov_b32_e32 v21, 1
	s_mov_b64 s[18:19], exec
	v_cmp_eq_u32_e32 vcc, 0, v1
	s_and_b64 exec, exec, vcc
	global_atomic_add v22, v20, v21, s[68:69] offset:256 sc0
	s_mov_b64 exec, s[18:19]
	s_waitcnt vmcnt(0)
	v_readfirstlane_b32 s40, v22
	s_cmp_lt_u32 s40, 0x3000
	s_cbranch_scc0 .Lcv_exit
	s_mov_b64 s[18:19], exec
	v_cmp_eq_u32_e32 vcc, 0, v1
	s_and_b64 exec, exec, vcc
	global_atomic_add v22, v20, v21, s[68:69] offset:256 sc0
	s_mov_b64 exec, s[18:19]
	s_waitcnt vmcnt(0)
	v_readfirstlane_b32 s22, v22
	s_mov_b64 s[18:19], exec
	v_cmp_eq_u32_e32 vcc, 0, v1
	s_and_b64 exec, exec, vcc
	global_atomic_add v22, v20, v21, s[68:69] offset:256 sc0
	s_mov_b64 exec, s[18:19]
	s_sub_u32 s1, 0x2fff, s40
	s_cmp_lt_u32 s1, 0x2000
	s_cbranch_scc0 .Lcv_dn_p
	s_lshr_b32 s2, s1, 8
	s_and_b32 s3, s1, 0xff
	s_lshr_b32 s4, s3, 4
	s_and_b32 s3, s3, 15
	s_lshl_b32 s5, s2, 25
	s_lshl_b32 s6, s4, 21
	s_add_u32 s5, s5, s6
	s_lshl_b32 s6, s3, 10
	s_add_u32 s5, s5, s6
	s_add_u32 s34, s42, s5
	s_addc_u32 s35, s43, 0
	s_lshl_b32 s5, s2, 23
	s_lshl_b32 s6, s3, 19
	s_add_u32 s5, s5, s6
	s_lshl_b32 s6, s4, 7
	s_add_u32 s5, s5, s6
	s_add_u32 s5, s5, 0x5e000000
	s_add_u32 s36, s68, s5
	s_addc_u32 s37, s69, 0
	s_movk_i32 s28, 0x4000
	s_mov_b32 s29, 0x60000
	s_movk_i32 s38, 0x2000
	s_mov_b32 s39, 0x10000
	s_mov_b32 s41, 1
	v_mov_b32_e32 v8, v6
	s_branch .Lcv_tp_p
.Lcv_dn_p:
	s_sub_u32 s1, s1, 0x2000
	s_lshr_b32 s2, s1, 7
	s_and_b32 s3, s1, 0x7f
	s_lshr_b32 s4, s3, 3
	s_and_b32 s3, s3, 7
	s_lshl_b32 s5, s2, 24
	s_lshl_b32 s6, s4, 20
	s_add_u32 s5, s5, s6
	s_lshl_b32 s6, s3, 10
	s_add_u32 s5, s5, s6
	s_add_u32 s34, s88, s5
	s_addc_u32 s35, s89, 0
	s_lshl_b32 s5, s2, 22
	s_lshl_b32 s6, s3, 19
	s_add_u32 s5, s5, s6
	s_lshl_b32 s6, s4, 7
	s_add_u32 s5, s5, s6
	s_add_u32 s5, s5, 0x7e000000
	s_add_u32 s36, s68, s5
	s_addc_u32 s37, s69, 0
	s_movk_i32 s28, 0x2000
	s_mov_b32 s29, 0x30000
	s_movk_i32 s38, 0x4000
	s_mov_b32 s39, 0x20000
	s_mov_b32 s41, 0
	v_mov_b32_e32 v8, v7
.Lcv_tp_p:
	s_mov_b64 s[32:33], s[36:37]
	s_mov_b32 s24, s38
	s_mov_b32 s25, s39
	s_mov_b32 s21, 0
	s_cmp_eq_u32 s41, 1
	s_cselect_b64 s[2:3], -1, 0
	s_nop 0
	v_cndmask_b32_e64 v11, v9, v10, s[2:3]
	s_mov_b32 s23, 1
	s_mov_b64 s[26:27], s[34:35]
	global_load_dwordx4 v[96:99], v8, s[26:27] nt
	s_add_u32 s26, s26, s28
	s_addc_u32 s27, s27, 0
	global_load_dwordx4 v[100:103], v8, s[26:27] nt
	s_add_u32 s26, s26, s28
	s_addc_u32 s27, s27, 0
	global_load_dwordx4 v[104:107], v8, s[26:27] nt
	s_add_u32 s26, s26, s28
	s_addc_u32 s27, s27, 0
	global_load_dwordx4 v[108:111], v8, s[26:27] nt
	s_add_u32 s26, s26, s28
	s_addc_u32 s27, s27, 0
	global_load_dwordx4 v[112:115], v8, s[26:27] nt
	s_add_u32 s26, s26, s28
	s_addc_u32 s27, s27, 0
	global_load_dwordx4 v[116:119], v8, s[26:27] nt
	s_add_u32 s26, s26, s28
	s_addc_u32 s27, s27, 0
	global_load_dwordx4 v[120:123], v8, s[26:27] nt
	s_add_u32 s26, s26, s28
	s_addc_u32 s27, s27, 0
	global_load_dwordx4 v[124:127], v8, s[26:27] nt
	s_add_u32 s26, s26, s28
	s_addc_u32 s27, s27, 0
	s_add_u32 s26, s26, s29
	s_addc_u32 s27, s27, 0
	global_load_dwordx4 v[128:131], v8, s[26:27] nt
	s_add_u32 s26, s26, s28
	s_addc_u32 s27, s27, 0
	global_load_dwordx4 v[132:135], v8, s[26:27] nt
	s_add_u32 s26, s26, s28
	s_addc_u32 s27, s27, 0
	global_load_dwordx4 v[136:139], v8, s[26:27] nt
	s_add_u32 s26, s26, s28
	s_addc_u32 s27, s27, 0
	global_load_dwordx4 v[140:143], v8, s[26:27] nt
	s_add_u32 s26, s26, s28
	s_addc_u32 s27, s27, 0
	global_load_dwordx4 v[144:147], v8, s[26:27] nt
	s_add_u32 s26, s26, s28
	s_addc_u32 s27, s27, 0
	global_load_dwordx4 v[148:151], v8, s[26:27] nt
	s_add_u32 s26, s26, s28
	s_addc_u32 s27, s27, 0
	global_load_dwordx4 v[152:155], v8, s[26:27] nt
	s_add_u32 s26, s26, s28
	s_addc_u32 s27, s27, 0
	global_load_dwordx4 v[156:159], v8, s[26:27] nt
	s_add_u32 s26, s26, s28
	s_addc_u32 s27, s27, 0
	s_add_u32 s26, s26, s29
	s_addc_u32 s27, s27, 0
	global_load_dwordx4 v[160:163], v8, s[26:27] nt
	s_add_u32 s26, s26, s28
	s_addc_u32 s27, s27, 0
	global_load_dwordx4 v[164:167], v8, s[26:27] nt
	s_add_u32 s26, s26, s28
	s_addc_u32 s27, s27, 0
	global_load_dwordx4 v[168:171], v8, s[26:27] nt
	s_add_u32 s26, s26, s28
	s_addc_u32 s27, s27, 0
	global_load_dwordx4 v[172:175], v8, s[26:27] nt
	s_add_u32 s26, s26, s28
	s_addc_u32 s27, s27, 0
	global_load_dwordx4 v[176:179], v8, s[26:27] nt
	s_add_u32 s26, s26, s28
	s_addc_u32 s27, s27, 0
	global_load_dwordx4 v[180:183], v8, s[26:27] nt
	s_add_u32 s26, s26, s28
	s_addc_u32 s27, s27, 0
	global_load_dwordx4 v[184:187], v8, s[26:27] nt
	s_add_u32 s26, s26, s28
	s_addc_u32 s27, s27, 0
	global_load_dwordx4 v[188:191], v8, s[26:27] nt
	s_add_u32 s26, s26, s28
	s_addc_u32 s27, s27, 0
	s_add_u32 s26, s26, s29
	s_addc_u32 s27, s27, 0
	global_load_dwordx4 v[192:195], v8, s[26:27] nt
	s_add_u32 s26, s26, s28
	s_addc_u32 s27, s27, 0
	global_load_dwordx4 v[196:199], v8, s[26:27] nt
	s_add_u32 s26, s26, s28
	s_addc_u32 s27, s27, 0
	global_load_dwordx4 v[200:203], v8, s[26:27] nt
	s_add_u32 s26, s26, s28
	s_addc_u32 s27, s27, 0
	global_load_dwordx4 v[204:207], v8, s[26:27] nt
	s_add_u32 s26, s26, s28
	s_addc_u32 s27, s27, 0
	global_load_dwordx4 v[208:211], v8, s[26:27] nt
	s_add_u32 s26, s26, s28
	s_addc_u32 s27, s27, 0
	global_load_dwordx4 v[212:215], v8, s[26:27] nt
	s_add_u32 s26, s26, s28
	s_addc_u32 s27, s27, 0
	global_load_dwordx4 v[216:219], v8, s[26:27] nt
	s_add_u32 s26, s26, s28
	s_addc_u32 s27, s27, 0
	global_load_dwordx4 v[220:223], v8, s[26:27] nt
	s_add_u32 s26, s26, s28
	s_addc_u32 s27, s27, 0
	s_add_u32 s26, s26, s29
	s_addc_u32 s27, s27, 0
	s_mov_b32 s20, 1
	s_add_u32 s34, s34, 0x100
	s_addc_u32 s35, s35, 0
	s_mov_b64 s[26:27], s[34:35]
	s_waitcnt vmcnt(24)
	v_pk_mul_f32 v[96:97], v[96:97], v[24:25]
	v_pk_mul_f32 v[98:99], v[98:99], v[24:25]
	v_pk_mul_f32 v[100:101], v[100:101], v[24:25]
	v_pk_mul_f32 v[102:103], v[102:103], v[24:25]
	v_pk_mul_f32 v[104:105], v[104:105], v[24:25]
	v_pk_mul_f32 v[106:107], v[106:107], v[24:25]
	v_pk_mul_f32 v[108:109], v[108:109], v[24:25]
	v_pk_mul_f32 v[110:111], v[110:111], v[24:25]
	v_pk_mul_f32 v[112:113], v[112:113], v[24:25]
	v_pk_mul_f32 v[114:115], v[114:115], v[24:25]
	v_pk_mul_f32 v[116:117], v[116:117], v[24:25]
	v_pk_mul_f32 v[118:119], v[118:119], v[24:25]
	v_pk_mul_f32 v[120:121], v[120:121], v[24:25]
	v_pk_mul_f32 v[122:123], v[122:123], v[24:25]
	v_pk_mul_f32 v[124:125], v[124:125], v[24:25]
	v_pk_mul_f32 v[126:127], v[126:127], v[24:25]
	v_cvt_pk_fp8_f32 v32, v96, v100
	v_cvt_pk_fp8_f32 v33, v112, v116
	v_cvt_pk_fp8_f32 v34, v97, v101
	v_cvt_pk_fp8_f32 v35, v113, v117
	v_cvt_pk_fp8_f32 v36, v98, v102
	v_cvt_pk_fp8_f32 v37, v114, v118
	v_cvt_pk_fp8_f32 v38, v99, v103
	v_cvt_pk_fp8_f32 v39, v115, v119
	v_cvt_pk_fp8_f32 v32, v104, v108 op_sel:[0,0,1]
	v_cvt_pk_fp8_f32 v33, v120, v124 op_sel:[0,0,1]
	v_cvt_pk_fp8_f32 v34, v105, v109 op_sel:[0,0,1]
	v_cvt_pk_fp8_f32 v35, v121, v125 op_sel:[0,0,1]
	v_cvt_pk_fp8_f32 v36, v106, v110 op_sel:[0,0,1]
	v_cvt_pk_fp8_f32 v37, v122, v126 op_sel:[0,0,1]
	v_cvt_pk_fp8_f32 v38, v107, v111 op_sel:[0,0,1]
	v_cvt_pk_fp8_f32 v39, v123, v127 op_sel:[0,0,1]
	s_nop 1
	ds_write_b64 v12, v[32:33]
	ds_write_b64 v12, v[34:35] offset:128
	ds_write_b64 v12, v[36:37] offset:256
	ds_write_b64 v12, v[38:39] offset:384
	global_load_dwordx4 v[96:99], v8, s[26:27] nt
	s_add_u32 s26, s26, s28
	s_addc_u32 s27, s27, 0
	global_load_dwordx4 v[100:103], v8, s[26:27] nt
	s_add_u32 s26, s26, s28
	s_addc_u32 s27, s27, 0
	global_load_dwordx4 v[104:107], v8, s[26:27] nt
	s_add_u32 s26, s26, s28
	s_addc_u32 s27, s27, 0
	global_load_dwordx4 v[108:111], v8, s[26:27] nt
	s_add_u32 s26, s26, s28
	s_addc_u32 s27, s27, 0
	global_load_dwordx4 v[112:115], v8, s[26:27] nt
	s_add_u32 s26, s26, s28
	s_addc_u32 s27, s27, 0
	global_load_dwordx4 v[116:119], v8, s[26:27] nt
	s_add_u32 s26, s26, s28
	s_addc_u32 s27, s27, 0
	global_load_dwordx4 v[120:123], v8, s[26:27] nt
	s_add_u32 s26, s26, s28
	s_addc_u32 s27, s27, 0
	global_load_dwordx4 v[124:127], v8, s[26:27] nt
	s_add_u32 s26, s26, s28
	s_addc_u32 s27, s27, 0
	s_add_u32 s26, s26, s29
	s_addc_u32 s27, s27, 0
	s_waitcnt vmcnt(24)
	v_pk_mul_f32 v[128:129], v[128:129], v[24:25]
	v_pk_mul_f32 v[130:131], v[130:131], v[24:25]
	v_pk_mul_f32 v[132:133], v[132:133], v[24:25]
	v_pk_mul_f32 v[134:135], v[134:135], v[24:25]
	v_pk_mul_f32 v[136:137], v[136:137], v[24:25]
	v_pk_mul_f32 v[138:139], v[138:139], v[24:25]
	v_pk_mul_f32 v[140:141], v[140:141], v[24:25]
	v_pk_mul_f32 v[142:143], v[142:143], v[24:25]
	v_pk_mul_f32 v[144:145], v[144:145], v[24:25]
	v_pk_mul_f32 v[146:147], v[146:147], v[24:25]
	v_pk_mul_f32 v[148:149], v[148:149], v[24:25]
	v_pk_mul_f32 v[150:151], v[150:151], v[24:25]
	v_pk_mul_f32 v[152:153], v[152:153], v[24:25]
	v_pk_mul_f32 v[154:155], v[154:155], v[24:25]
	v_pk_mul_f32 v[156:157], v[156:157], v[24:25]
	v_pk_mul_f32 v[158:159], v[158:159], v[24:25]
	v_cvt_pk_fp8_f32 v40, v128, v132
	v_cvt_pk_fp8_f32 v41, v144, v148
	v_cvt_pk_fp8_f32 v42, v129, v133
	v_cvt_pk_fp8_f32 v43, v145, v149
	v_cvt_pk_fp8_f32 v44, v130, v134
	v_cvt_pk_fp8_f32 v45, v146, v150
	v_cvt_pk_fp8_f32 v46, v131, v135
	v_cvt_pk_fp8_f32 v47, v147, v151
	v_cvt_pk_fp8_f32 v40, v136, v140 op_sel:[0,0,1]
	v_cvt_pk_fp8_f32 v41, v152, v156 op_sel:[0,0,1]
	v_cvt_pk_fp8_f32 v42, v137, v141 op_sel:[0,0,1]
	v_cvt_pk_fp8_f32 v43, v153, v157 op_sel:[0,0,1]
	v_cvt_pk_fp8_f32 v44, v138, v142 op_sel:[0,0,1]
	v_cvt_pk_fp8_f32 v45, v154, v158 op_sel:[0,0,1]
	v_cvt_pk_fp8_f32 v46, v139, v143 op_sel:[0,0,1]
	v_cvt_pk_fp8_f32 v47, v155, v159 op_sel:[0,0,1]
	s_nop 1
	ds_write_b64 v13, v[40:41]
	ds_write_b64 v13, v[42:43] offset:128
	ds_write_b64 v13, v[44:45] offset:256
	ds_write_b64 v13, v[46:47] offset:384
	global_load_dwordx4 v[128:131], v8, s[26:27] nt
	s_add_u32 s26, s26, s28
	s_addc_u32 s27, s27, 0
	global_load_dwordx4 v[132:135], v8, s[26:27] nt
	s_add_u32 s26, s26, s28
	s_addc_u32 s27, s27, 0
	global_load_dwordx4 v[136:139], v8, s[26:27] nt
	s_add_u32 s26, s26, s28
	s_addc_u32 s27, s27, 0
	global_load_dwordx4 v[140:143], v8, s[26:27] nt
	s_add_u32 s26, s26, s28
	s_addc_u32 s27, s27, 0
	global_load_dwordx4 v[144:147], v8, s[26:27] nt
	s_add_u32 s26, s26, s28
	s_addc_u32 s27, s27, 0
	global_load_dwordx4 v[148:151], v8, s[26:27] nt
	s_add_u32 s26, s26, s28
	s_addc_u32 s27, s27, 0
	global_load_dwordx4 v[152:155], v8, s[26:27] nt
	s_add_u32 s26, s26, s28
	s_addc_u32 s27, s27, 0
	global_load_dwordx4 v[156:159], v8, s[26:27] nt
	s_add_u32 s26, s26, s28
	s_addc_u32 s27, s27, 0
	s_add_u32 s26, s26, s29
	s_addc_u32 s27, s27, 0
	s_waitcnt vmcnt(24)
	v_pk_mul_f32 v[160:161], v[160:161], v[24:25]
	v_pk_mul_f32 v[162:163], v[162:163], v[24:25]
	v_pk_mul_f32 v[164:165], v[164:165], v[24:25]
	v_pk_mul_f32 v[166:167], v[166:167], v[24:25]
	v_pk_mul_f32 v[168:169], v[168:169], v[24:25]
	v_pk_mul_f32 v[170:171], v[170:171], v[24:25]
	v_pk_mul_f32 v[172:173], v[172:173], v[24:25]
	v_pk_mul_f32 v[174:175], v[174:175], v[24:25]
	v_pk_mul_f32 v[176:177], v[176:177], v[24:25]
	v_pk_mul_f32 v[178:179], v[178:179], v[24:25]
	v_pk_mul_f32 v[180:181], v[180:181], v[24:25]
	v_pk_mul_f32 v[182:183], v[182:183], v[24:25]
	v_pk_mul_f32 v[184:185], v[184:185], v[24:25]
	v_pk_mul_f32 v[186:187], v[186:187], v[24:25]
	v_pk_mul_f32 v[188:189], v[188:189], v[24:25]
	v_pk_mul_f32 v[190:191], v[190:191], v[24:25]
	v_cvt_pk_fp8_f32 v32, v160, v164
	v_cvt_pk_fp8_f32 v33, v176, v180
	v_cvt_pk_fp8_f32 v34, v161, v165
	v_cvt_pk_fp8_f32 v35, v177, v181
	v_cvt_pk_fp8_f32 v36, v162, v166
	v_cvt_pk_fp8_f32 v37, v178, v182
	v_cvt_pk_fp8_f32 v38, v163, v167
	v_cvt_pk_fp8_f32 v39, v179, v183
	v_cvt_pk_fp8_f32 v32, v168, v172 op_sel:[0,0,1]
	v_cvt_pk_fp8_f32 v33, v184, v188 op_sel:[0,0,1]
	v_cvt_pk_fp8_f32 v34, v169, v173 op_sel:[0,0,1]
	v_cvt_pk_fp8_f32 v35, v185, v189 op_sel:[0,0,1]
	v_cvt_pk_fp8_f32 v36, v170, v174 op_sel:[0,0,1]
	v_cvt_pk_fp8_f32 v37, v186, v190 op_sel:[0,0,1]
	v_cvt_pk_fp8_f32 v38, v171, v175 op_sel:[0,0,1]
	v_cvt_pk_fp8_f32 v39, v187, v191 op_sel:[0,0,1]
	s_nop 1
	ds_write_b64 v14, v[32:33]
	ds_write_b64 v14, v[34:35] offset:128
	ds_write_b64 v14, v[36:37] offset:256
	ds_write_b64 v14, v[38:39] offset:384
	global_load_dwordx4 v[160:163], v8, s[26:27] nt
	s_add_u32 s26, s26, s28
	s_addc_u32 s27, s27, 0
	global_load_dwordx4 v[164:167], v8, s[26:27] nt
	s_add_u32 s26, s26, s28
	s_addc_u32 s27, s27, 0
	global_load_dwordx4 v[168:171], v8, s[26:27] nt
	s_add_u32 s26, s26, s28
	s_addc_u32 s27, s27, 0
	global_load_dwordx4 v[172:175], v8, s[26:27] nt
	s_add_u32 s26, s26, s28
	s_addc_u32 s27, s27, 0
	global_load_dwordx4 v[176:179], v8, s[26:27] nt
	s_add_u32 s26, s26, s28
	s_addc_u32 s27, s27, 0
	global_load_dwordx4 v[180:183], v8, s[26:27] nt
	s_add_u32 s26, s26, s28
	s_addc_u32 s27, s27, 0
	global_load_dwordx4 v[184:187], v8, s[26:27] nt
	s_add_u32 s26, s26, s28
	s_addc_u32 s27, s27, 0
	global_load_dwordx4 v[188:191], v8, s[26:27] nt
	s_add_u32 s26, s26, s28
	s_addc_u32 s27, s27, 0
	s_add_u32 s26, s26, s29
	s_addc_u32 s27, s27, 0
	s_waitcnt vmcnt(24)
	v_pk_mul_f32 v[192:193], v[192:193], v[24:25]
	v_pk_mul_f32 v[194:195], v[194:195], v[24:25]
	v_pk_mul_f32 v[196:197], v[196:197], v[24:25]
	v_pk_mul_f32 v[198:199], v[198:199], v[24:25]
	v_pk_mul_f32 v[200:201], v[200:201], v[24:25]
	v_pk_mul_f32 v[202:203], v[202:203], v[24:25]
	v_pk_mul_f32 v[204:205], v[204:205], v[24:25]
	v_pk_mul_f32 v[206:207], v[206:207], v[24:25]
	v_pk_mul_f32 v[208:209], v[208:209], v[24:25]
	v_pk_mul_f32 v[210:211], v[210:211], v[24:25]
	v_pk_mul_f32 v[212:213], v[212:213], v[24:25]
	v_pk_mul_f32 v[214:215], v[214:215], v[24:25]
	v_pk_mul_f32 v[216:217], v[216:217], v[24:25]
	v_pk_mul_f32 v[218:219], v[218:219], v[24:25]
	v_pk_mul_f32 v[220:221], v[220:221], v[24:25]
	v_pk_mul_f32 v[222:223], v[222:223], v[24:25]
	v_cvt_pk_fp8_f32 v40, v192, v196
	v_cvt_pk_fp8_f32 v41, v208, v212
	v_cvt_pk_fp8_f32 v42, v193, v197
	v_cvt_pk_fp8_f32 v43, v209, v213
	v_cvt_pk_fp8_f32 v44, v194, v198
	v_cvt_pk_fp8_f32 v45, v210, v214
	v_cvt_pk_fp8_f32 v46, v195, v199
	v_cvt_pk_fp8_f32 v47, v211, v215
	v_cvt_pk_fp8_f32 v40, v200, v204 op_sel:[0,0,1]
	v_cvt_pk_fp8_f32 v41, v216, v220 op_sel:[0,0,1]
	v_cvt_pk_fp8_f32 v42, v201, v205 op_sel:[0,0,1]
	v_cvt_pk_fp8_f32 v43, v217, v221 op_sel:[0,0,1]
	v_cvt_pk_fp8_f32 v44, v202, v206 op_sel:[0,0,1]
	v_cvt_pk_fp8_f32 v45, v218, v222 op_sel:[0,0,1]
	v_cvt_pk_fp8_f32 v46, v203, v207 op_sel:[0,0,1]
	v_cvt_pk_fp8_f32 v47, v219, v223 op_sel:[0,0,1]
	s_nop 1
	ds_write_b64 v15, v[40:41]
	ds_write_b64 v15, v[42:43] offset:128
	ds_write_b64 v15, v[44:45] offset:256
	ds_write_b64 v15, v[46:47] offset:384
	global_load_dwordx4 v[192:195], v8, s[26:27] nt
	s_add_u32 s26, s26, s28
	s_addc_u32 s27, s27, 0
	global_load_dwordx4 v[196:199], v8, s[26:27] nt
	s_add_u32 s26, s26, s28
	s_addc_u32 s27, s27, 0
	global_load_dwordx4 v[200:203], v8, s[26:27] nt
	s_add_u32 s26, s26, s28
	s_addc_u32 s27, s27, 0
	global_load_dwordx4 v[204:207], v8, s[26:27] nt
	s_add_u32 s26, s26, s28
	s_addc_u32 s27, s27, 0
	global_load_dwordx4 v[208:211], v8, s[26:27] nt
	s_add_u32 s26, s26, s28
	s_addc_u32 s27, s27, 0
	global_load_dwordx4 v[212:215], v8, s[26:27] nt
	s_add_u32 s26, s26, s28
	s_addc_u32 s27, s27, 0
	global_load_dwordx4 v[216:219], v8, s[26:27] nt
	s_add_u32 s26, s26, s28
	s_addc_u32 s27, s27, 0
	global_load_dwordx4 v[220:223], v8, s[26:27] nt
	s_add_u32 s26, s26, s28
	s_addc_u32 s27, s27, 0
	s_add_u32 s26, s26, s29
	s_addc_u32 s27, s27, 0
	s_mov_b64 s[30:31], s[32:33]
	ds_read_b128 v[48:51], v16
	ds_read_b128 v[52:55], v17 offset:1024
	ds_read_b128 v[56:59], v18 offset:2048
	ds_read_b128 v[60:63], v19 offset:3072
	ds_read_b128 v[64:67], v16 offset:4096
	ds_read_b128 v[68:71], v17 offset:5120
	ds_read_b128 v[72:75], v18 offset:6144
	ds_read_b128 v[76:79], v19 offset:7168
	s_waitcnt lgkmcnt(7)
	global_store_dwordx4 v11, v[48:51], s[30:31] nt
	s_add_u32 s30, s30, s24
	s_addc_u32 s31, s31, 0
	s_waitcnt lgkmcnt(6)
	global_store_dwordx4 v11, v[52:55], s[30:31] nt
	s_add_u32 s30, s30, s24
	s_addc_u32 s31, s31, 0
	s_waitcnt lgkmcnt(5)
	global_store_dwordx4 v11, v[56:59], s[30:31] nt
	s_add_u32 s30, s30, s24
	s_addc_u32 s31, s31, 0
	s_waitcnt lgkmcnt(4)
	global_store_dwordx4 v11, v[60:63], s[30:31] nt
	s_add_u32 s30, s30, s24
	s_addc_u32 s31, s31, 0
	s_waitcnt lgkmcnt(3)
	global_store_dwordx4 v11, v[64:67], s[30:31] nt
	s_add_u32 s30, s30, s24
	s_addc_u32 s31, s31, 0
	s_waitcnt lgkmcnt(2)
	global_store_dwordx4 v11, v[68:71], s[30:31] nt
	s_add_u32 s30, s30, s24
	s_addc_u32 s31, s31, 0
	s_waitcnt lgkmcnt(1)
	global_store_dwordx4 v11, v[72:75], s[30:31] nt
	s_add_u32 s30, s30, s24
	s_addc_u32 s31, s31, 0
	s_waitcnt lgkmcnt(0)
	global_store_dwordx4 v11, v[76:79], s[30:31] nt
	s_add_u32 s30, s30, s24
	s_addc_u32 s31, s31, 0
	s_add_u32 s21, s21, 1
	s_cmp_lt_u32 s21, 4
	s_cbranch_scc1 .Lcv_stin_f
	s_mov_b32 s21, 0
	s_mov_b64 s[32:33], s[36:37]
	s_mov_b32 s24, s38
	s_mov_b32 s25, s39
	s_cmp_eq_u32 s41, 1
	s_cselect_b64 s[2:3], -1, 0
	s_nop 0
	v_cndmask_b32_e64 v11, v9, v10, s[2:3]
	s_branch .Lcv_stdn_f
.Lcv_stin_f:
	s_add_u32 s32, s32, s25
	s_addc_u32 s33, s33, 0
.Lcv_stdn_f:
	s_add_u32 s20, s20, 1
	s_cmp_lt_u32 s20, 4
	s_cbranch_scc1 .Lcv_ldin_f
	s_cmp_lt_u32 s22, 0x3000
	s_cbranch_scc0 .Lcv_ldno_f
	s_mov_b32 s40, s22
	v_readfirstlane_b32 s22, v22
	s_sub_u32 s1, 0x2fff, s40
	s_cmp_lt_u32 s1, 0x2000
	s_cbranch_scc0 .Lcv_dn_f
	s_lshr_b32 s2, s1, 8
	s_and_b32 s3, s1, 0xff
	s_lshr_b32 s4, s3, 4
	s_and_b32 s3, s3, 15
	s_lshl_b32 s5, s2, 25
	s_lshl_b32 s6, s4, 21
	s_add_u32 s5, s5, s6
	s_lshl_b32 s6, s3, 10
	s_add_u32 s5, s5, s6
	s_add_u32 s34, s42, s5
	s_addc_u32 s35, s43, 0
	s_lshl_b32 s5, s2, 23
	s_lshl_b32 s6, s3, 19
	s_add_u32 s5, s5, s6
	s_lshl_b32 s6, s4, 7
	s_add_u32 s5, s5, s6
	s_add_u32 s5, s5, 0x5e000000
	s_add_u32 s36, s68, s5
	s_addc_u32 s37, s69, 0
	s_movk_i32 s28, 0x4000
	s_mov_b32 s29, 0x60000
	s_movk_i32 s38, 0x2000
	s_mov_b32 s39, 0x10000
	s_mov_b32 s41, 1
	v_mov_b32_e32 v8, v6
	s_branch .Lcv_tp_f

.Lcv_tp_f:
	s_mov_b64 s[18:19], exec
	v_cmp_eq_u32_e32 vcc, 0, v1
	s_and_b64 exec, exec, vcc
	global_atomic_add v22, v20, v21, s[68:69] offset:256 sc0
	s_mov_b64 exec, s[18:19]
	s_mov_b32 s20, 0
	s_branch .Lcv_lddn_f
.Lcv_ldno_f:
	s_mov_b32 s23, 0
	s_branch .Lcv_lddn_f
.Lcv_ldin_f:
	s_add_u32 s34, s34, 0x100
	s_addc_u32 s35, s35, 0
.Lcv_lddn_f:
.Lcv_loop:
	s_cmp_eq_u32 s23, 0
	s_cbranch_scc1 .Lcv_final
	s_mov_b64 s[26:27], s[34:35]
	s_waitcnt vmcnt(32)
	v_pk_mul_f32 v[96:97], v[96:97], v[24:25]
	v_pk_mul_f32 v[98:99], v[98:99], v[24:25]
	v_pk_mul_f32 v[100:101], v[100:101], v[24:25]
	v_pk_mul_f32 v[102:103], v[102:103], v[24:25]
	v_pk_mul_f32 v[104:105], v[104:105], v[24:25]
	v_pk_mul_f32 v[106:107], v[106:107], v[24:25]
	v_pk_mul_f32 v[108:109], v[108:109], v[24:25]
	v_pk_mul_f32 v[110:111], v[110:111], v[24:25]
	v_pk_mul_f32 v[112:113], v[112:113], v[24:25]
	v_pk_mul_f32 v[114:115], v[114:115], v[24:25]
	v_pk_mul_f32 v[116:117], v[116:117], v[24:25]
	v_pk_mul_f32 v[118:119], v[118:119], v[24:25]
	v_pk_mul_f32 v[120:121], v[120:121], v[24:25]
	v_pk_mul_f32 v[122:123], v[122:123], v[24:25]
	v_pk_mul_f32 v[124:125], v[124:125], v[24:25]
	v_pk_mul_f32 v[126:127], v[126:127], v[24:25]
	v_cvt_pk_fp8_f32 v32, v96, v100
	v_cvt_pk_fp8_f32 v33, v112, v116
	v_cvt_pk_fp8_f32 v34, v97, v101
	v_cvt_pk_fp8_f32 v35, v113, v117
	v_cvt_pk_fp8_f32 v36, v98, v102
	v_cvt_pk_fp8_f32 v37, v114, v118
	v_cvt_pk_fp8_f32 v38, v99, v103
	v_cvt_pk_fp8_f32 v39, v115, v119
	v_cvt_pk_fp8_f32 v32, v104, v108 op_sel:[0,0,1]
	v_cvt_pk_fp8_f32 v33, v120, v124 op_sel:[0,0,1]
	v_cvt_pk_fp8_f32 v34, v105, v109 op_sel:[0,0,1]
	v_cvt_pk_fp8_f32 v35, v121, v125 op_sel:[0,0,1]
	v_cvt_pk_fp8_f32 v36, v106, v110 op_sel:[0,0,1]
	v_cvt_pk_fp8_f32 v37, v122, v126 op_sel:[0,0,1]
	v_cvt_pk_fp8_f32 v38, v107, v111 op_sel:[0,0,1]
	v_cvt_pk_fp8_f32 v39, v123, v127 op_sel:[0,0,1]
	s_nop 1
	ds_write_b64 v12, v[32:33]
	ds_write_b64 v12, v[34:35] offset:128
	ds_write_b64 v12, v[36:37] offset:256
	ds_write_b64 v12, v[38:39] offset:384
	global_load_dwordx4 v[96:99], v8, s[26:27] nt
	s_add_u32 s26, s26, s28
	s_addc_u32 s27, s27, 0
	global_load_dwordx4 v[100:103], v8, s[26:27] nt
	s_add_u32 s26, s26, s28
	s_addc_u32 s27, s27, 0
	global_load_dwordx4 v[104:107], v8, s[26:27] nt
	s_add_u32 s26, s26, s28
	s_addc_u32 s27, s27, 0
	global_load_dwordx4 v[108:111], v8, s[26:27] nt
	s_add_u32 s26, s26, s28
	s_addc_u32 s27, s27, 0
	global_load_dwordx4 v[112:115], v8, s[26:27] nt
	s_add_u32 s26, s26, s28
	s_addc_u32 s27, s27, 0
	global_load_dwordx4 v[116:119], v8, s[26:27] nt
	s_add_u32 s26, s26, s28
	s_addc_u32 s27, s27, 0
	global_load_dwordx4 v[120:123], v8, s[26:27] nt
	s_add_u32 s26, s26, s28
	s_addc_u32 s27, s27, 0
	global_load_dwordx4 v[124:127], v8, s[26:27] nt
	s_add_u32 s26, s26, s28
	s_addc_u32 s27, s27, 0
	s_add_u32 s26, s26, s29
	s_addc_u32 s27, s27, 0
	s_waitcnt vmcnt(32)
	v_pk_mul_f32 v[128:129], v[128:129], v[24:25]
	v_pk_mul_f32 v[130:131], v[130:131], v[24:25]
	v_pk_mul_f32 v[132:133], v[132:133], v[24:25]
	v_pk_mul_f32 v[134:135], v[134:135], v[24:25]
	v_pk_mul_f32 v[136:137], v[136:137], v[24:25]
	v_pk_mul_f32 v[138:139], v[138:139], v[24:25]
	v_pk_mul_f32 v[140:141], v[140:141], v[24:25]
	v_pk_mul_f32 v[142:143], v[142:143], v[24:25]
	v_pk_mul_f32 v[144:145], v[144:145], v[24:25]
	v_pk_mul_f32 v[146:147], v[146:147], v[24:25]
	v_pk_mul_f32 v[148:149], v[148:149], v[24:25]
	v_pk_mul_f32 v[150:151], v[150:151], v[24:25]
	v_pk_mul_f32 v[152:153], v[152:153], v[24:25]
	v_pk_mul_f32 v[154:155], v[154:155], v[24:25]
	v_pk_mul_f32 v[156:157], v[156:157], v[24:25]
	v_pk_mul_f32 v[158:159], v[158:159], v[24:25]
	v_cvt_pk_fp8_f32 v40, v128, v132
	v_cvt_pk_fp8_f32 v41, v144, v148
	v_cvt_pk_fp8_f32 v42, v129, v133
	v_cvt_pk_fp8_f32 v43, v145, v149
	v_cvt_pk_fp8_f32 v44, v130, v134
	v_cvt_pk_fp8_f32 v45, v146, v150
	v_cvt_pk_fp8_f32 v46, v131, v135
	v_cvt_pk_fp8_f32 v47, v147, v151
	v_cvt_pk_fp8_f32 v40, v136, v140 op_sel:[0,0,1]
	v_cvt_pk_fp8_f32 v41, v152, v156 op_sel:[0,0,1]
	v_cvt_pk_fp8_f32 v42, v137, v141 op_sel:[0,0,1]
	v_cvt_pk_fp8_f32 v43, v153, v157 op_sel:[0,0,1]
	v_cvt_pk_fp8_f32 v44, v138, v142 op_sel:[0,0,1]
	v_cvt_pk_fp8_f32 v45, v154, v158 op_sel:[0,0,1]
	v_cvt_pk_fp8_f32 v46, v139, v143 op_sel:[0,0,1]
	v_cvt_pk_fp8_f32 v47, v155, v159 op_sel:[0,0,1]
	s_nop 1
	ds_write_b64 v13, v[40:41]
	ds_write_b64 v13, v[42:43] offset:128
	ds_write_b64 v13, v[44:45] offset:256
	ds_write_b64 v13, v[46:47] offset:384
	global_load_dwordx4 v[128:131], v8, s[26:27] nt
	s_add_u32 s26, s26, s28
	s_addc_u32 s27, s27, 0
	global_load_dwordx4 v[132:135], v8, s[26:27] nt
	s_add_u32 s26, s26, s28
	s_addc_u32 s27, s27, 0
	global_load_dwordx4 v[136:139], v8, s[26:27] nt
	s_add_u32 s26, s26, s28
	s_addc_u32 s27, s27, 0
	global_load_dwordx4 v[140:143], v8, s[26:27] nt
	s_add_u32 s26, s26, s28
	s_addc_u32 s27, s27, 0
	global_load_dwordx4 v[144:147], v8, s[26:27] nt
	s_add_u32 s26, s26, s28
	s_addc_u32 s27, s27, 0
	global_load_dwordx4 v[148:151], v8, s[26:27] nt
	s_add_u32 s26, s26, s28
	s_addc_u32 s27, s27, 0
	global_load_dwordx4 v[152:155], v8, s[26:27] nt
	s_add_u32 s26, s26, s28
	s_addc_u32 s27, s27, 0
	global_load_dwordx4 v[156:159], v8, s[26:27] nt
	s_add_u32 s26, s26, s28
	s_addc_u32 s27, s27, 0
	s_add_u32 s26, s26, s29
	s_addc_u32 s27, s27, 0
	s_waitcnt vmcnt(32)
	v_pk_mul_f32 v[160:161], v[160:161], v[24:25]
	v_pk_mul_f32 v[162:163], v[162:163], v[24:25]
	v_pk_mul_f32 v[164:165], v[164:165], v[24:25]
	v_pk_mul_f32 v[166:167], v[166:167], v[24:25]
	v_pk_mul_f32 v[168:169], v[168:169], v[24:25]
	v_pk_mul_f32 v[170:171], v[170:171], v[24:25]
	v_pk_mul_f32 v[172:173], v[172:173], v[24:25]
	v_pk_mul_f32 v[174:175], v[174:175], v[24:25]
	v_pk_mul_f32 v[176:177], v[176:177], v[24:25]
	v_pk_mul_f32 v[178:179], v[178:179], v[24:25]
	v_pk_mul_f32 v[180:181], v[180:181], v[24:25]
	v_pk_mul_f32 v[182:183], v[182:183], v[24:25]
	v_pk_mul_f32 v[184:185], v[184:185], v[24:25]
	v_pk_mul_f32 v[186:187], v[186:187], v[24:25]
	v_pk_mul_f32 v[188:189], v[188:189], v[24:25]
	v_pk_mul_f32 v[190:191], v[190:191], v[24:25]
	v_cvt_pk_fp8_f32 v32, v160, v164
	v_cvt_pk_fp8_f32 v33, v176, v180
	v_cvt_pk_fp8_f32 v34, v161, v165
	v_cvt_pk_fp8_f32 v35, v177, v181
	v_cvt_pk_fp8_f32 v36, v162, v166
	v_cvt_pk_fp8_f32 v37, v178, v182
	v_cvt_pk_fp8_f32 v38, v163, v167
	v_cvt_pk_fp8_f32 v39, v179, v183
	v_cvt_pk_fp8_f32 v32, v168, v172 op_sel:[0,0,1]
	v_cvt_pk_fp8_f32 v33, v184, v188 op_sel:[0,0,1]
	v_cvt_pk_fp8_f32 v34, v169, v173 op_sel:[0,0,1]
	v_cvt_pk_fp8_f32 v35, v185, v189 op_sel:[0,0,1]
	v_cvt_pk_fp8_f32 v36, v170, v174 op_sel:[0,0,1]
	v_cvt_pk_fp8_f32 v37, v186, v190 op_sel:[0,0,1]
	v_cvt_pk_fp8_f32 v38, v171, v175 op_sel:[0,0,1]
	v_cvt_pk_fp8_f32 v39, v187, v191 op_sel:[0,0,1]
	s_nop 1
	ds_write_b64 v14, v[32:33]
	ds_write_b64 v14, v[34:35] offset:128
	ds_write_b64 v14, v[36:37] offset:256
	ds_write_b64 v14, v[38:39] offset:384
	global_load_dwordx4 v[160:163], v8, s[26:27] nt
	s_add_u32 s26, s26, s28
	s_addc_u32 s27, s27, 0
	global_load_dwordx4 v[164:167], v8, s[26:27] nt
	s_add_u32 s26, s26, s28
	s_addc_u32 s27, s27, 0
	global_load_dwordx4 v[168:171], v8, s[26:27] nt
	s_add_u32 s26, s26, s28
	s_addc_u32 s27, s27, 0
	global_load_dwordx4 v[172:175], v8, s[26:27] nt
	s_add_u32 s26, s26, s28
	s_addc_u32 s27, s27, 0
	global_load_dwordx4 v[176:179], v8, s[26:27] nt
	s_add_u32 s26, s26, s28
	s_addc_u32 s27, s27, 0
	global_load_dwordx4 v[180:183], v8, s[26:27] nt
	s_add_u32 s26, s26, s28
	s_addc_u32 s27, s27, 0
	global_load_dwordx4 v[184:187], v8, s[26:27] nt
	s_add_u32 s26, s26, s28
	s_addc_u32 s27, s27, 0
	global_load_dwordx4 v[188:191], v8, s[26:27] nt
	s_add_u32 s26, s26, s28
	s_addc_u32 s27, s27, 0
	s_add_u32 s26, s26, s29
	s_addc_u32 s27, s27, 0
	s_waitcnt vmcnt(32)
	v_pk_mul_f32 v[192:193], v[192:193], v[24:25]
	v_pk_mul_f32 v[194:195], v[194:195], v[24:25]
	v_pk_mul_f32 v[196:197], v[196:197], v[24:25]
	v_pk_mul_f32 v[198:199], v[198:199], v[24:25]
	v_pk_mul_f32 v[200:201], v[200:201], v[24:25]
	v_pk_mul_f32 v[202:203], v[202:203], v[24:25]
	v_pk_mul_f32 v[204:205], v[204:205], v[24:25]
	v_pk_mul_f32 v[206:207], v[206:207], v[24:25]
	v_pk_mul_f32 v[208:209], v[208:209], v[24:25]
	v_pk_mul_f32 v[210:211], v[210:211], v[24:25]
	v_pk_mul_f32 v[212:213], v[212:213], v[24:25]
	v_pk_mul_f32 v[214:215], v[214:215], v[24:25]
	v_pk_mul_f32 v[216:217], v[216:217], v[24:25]
	v_pk_mul_f32 v[218:219], v[218:219], v[24:25]
	v_pk_mul_f32 v[220:221], v[220:221], v[24:25]
	v_pk_mul_f32 v[222:223], v[222:223], v[24:25]
	v_cvt_pk_fp8_f32 v40, v192, v196
	v_cvt_pk_fp8_f32 v41, v208, v212
	v_cvt_pk_fp8_f32 v42, v193, v197
	v_cvt_pk_fp8_f32 v43, v209, v213
	v_cvt_pk_fp8_f32 v44, v194, v198
	v_cvt_pk_fp8_f32 v45, v210, v214
	v_cvt_pk_fp8_f32 v46, v195, v199
	v_cvt_pk_fp8_f32 v47, v211, v215
	v_cvt_pk_fp8_f32 v40, v200, v204 op_sel:[0,0,1]
	v_cvt_pk_fp8_f32 v41, v216, v220 op_sel:[0,0,1]
	v_cvt_pk_fp8_f32 v42, v201, v205 op_sel:[0,0,1]
	v_cvt_pk_fp8_f32 v43, v217, v221 op_sel:[0,0,1]
	v_cvt_pk_fp8_f32 v44, v202, v206 op_sel:[0,0,1]
	v_cvt_pk_fp8_f32 v45, v218, v222 op_sel:[0,0,1]
	v_cvt_pk_fp8_f32 v46, v203, v207 op_sel:[0,0,1]
	v_cvt_pk_fp8_f32 v47, v219, v223 op_sel:[0,0,1]
	s_nop 1
	ds_write_b64 v15, v[40:41]
	ds_write_b64 v15, v[42:43] offset:128
	ds_write_b64 v15, v[44:45] offset:256
	ds_write_b64 v15, v[46:47] offset:384
	global_load_dwordx4 v[192:195], v8, s[26:27] nt
	s_add_u32 s26, s26, s28
	s_addc_u32 s27, s27, 0
	global_load_dwordx4 v[196:199], v8, s[26:27] nt
	s_add_u32 s26, s26, s28
	s_addc_u32 s27, s27, 0
	global_load_dwordx4 v[200:203], v8, s[26:27] nt
	s_add_u32 s26, s26, s28
	s_addc_u32 s27, s27, 0
	global_load_dwordx4 v[204:207], v8, s[26:27] nt
	s_add_u32 s26, s26, s28
	s_addc_u32 s27, s27, 0
	global_load_dwordx4 v[208:211], v8, s[26:27] nt
	s_add_u32 s26, s26, s28
	s_addc_u32 s27, s27, 0
	global_load_dwordx4 v[212:215], v8, s[26:27] nt
	s_add_u32 s26, s26, s28
	s_addc_u32 s27, s27, 0
	global_load_dwordx4 v[216:219], v8, s[26:27] nt
	s_add_u32 s26, s26, s28
	s_addc_u32 s27, s27, 0
	global_load_dwordx4 v[220:223], v8, s[26:27] nt
	s_add_u32 s26, s26, s28
	s_addc_u32 s27, s27, 0
	s_add_u32 s26, s26, s29
	s_addc_u32 s27, s27, 0
	s_mov_b64 s[30:31], s[32:33]
	ds_read_b128 v[48:51], v16
	ds_read_b128 v[52:55], v17 offset:1024
	ds_read_b128 v[56:59], v18 offset:2048
	ds_read_b128 v[60:63], v19 offset:3072
	ds_read_b128 v[64:67], v16 offset:4096
	ds_read_b128 v[68:71], v17 offset:5120
	ds_read_b128 v[72:75], v18 offset:6144
	ds_read_b128 v[76:79], v19 offset:7168
	s_waitcnt lgkmcnt(7)
	global_store_dwordx4 v11, v[48:51], s[30:31] nt
	s_add_u32 s30, s30, s24
	s_addc_u32 s31, s31, 0
	s_waitcnt lgkmcnt(6)
	global_store_dwordx4 v11, v[52:55], s[30:31] nt
	s_add_u32 s30, s30, s24
	s_addc_u32 s31, s31, 0
	s_waitcnt lgkmcnt(5)
	global_store_dwordx4 v11, v[56:59], s[30:31] nt
	s_add_u32 s30, s30, s24
	s_addc_u32 s31, s31, 0
	s_waitcnt lgkmcnt(4)
	global_store_dwordx4 v11, v[60:63], s[30:31] nt
	s_add_u32 s30, s30, s24
	s_addc_u32 s31, s31, 0
	s_waitcnt lgkmcnt(3)
	global_store_dwordx4 v11, v[64:67], s[30:31] nt
	s_add_u32 s30, s30, s24
	s_addc_u32 s31, s31, 0
	s_waitcnt lgkmcnt(2)
	global_store_dwordx4 v11, v[68:71], s[30:31] nt
	s_add_u32 s30, s30, s24
	s_addc_u32 s31, s31, 0
	s_waitcnt lgkmcnt(1)
	global_store_dwordx4 v11, v[72:75], s[30:31] nt
	s_add_u32 s30, s30, s24
	s_addc_u32 s31, s31, 0
	s_waitcnt lgkmcnt(0)
	global_store_dwordx4 v11, v[76:79], s[30:31] nt
	s_add_u32 s30, s30, s24
	s_addc_u32 s31, s31, 0
	s_add_u32 s21, s21, 1
	s_cmp_lt_u32 s21, 4
	s_cbranch_scc1 .Lcv_stin_s
	s_mov_b32 s21, 0
	s_mov_b64 s[32:33], s[36:37]
	s_mov_b32 s24, s38
	s_mov_b32 s25, s39
	s_cmp_eq_u32 s41, 1
	s_cselect_b64 s[2:3], -1, 0
	s_nop 0
	v_cndmask_b32_e64 v11, v9, v10, s[2:3]
	s_branch .Lcv_stdn_s

.Lcv_final:
	s_waitcnt vmcnt(24)
	v_pk_mul_f32 v[96:97], v[96:97], v[24:25]
	v_pk_mul_f32 v[98:99], v[98:99], v[24:25]
	v_pk_mul_f32 v[100:101], v[100:101], v[24:25]
	v_pk_mul_f32 v[102:103], v[102:103], v[24:25]
	v_pk_mul_f32 v[104:105], v[104:105], v[24:25]
	v_pk_mul_f32 v[106:107], v[106:107], v[24:25]
	v_pk_mul_f32 v[108:109], v[108:109], v[24:25]
	v_pk_mul_f32 v[110:111], v[110:111], v[24:25]
	v_pk_mul_f32 v[112:113], v[112:113], v[24:25]
	v_pk_mul_f32 v[114:115], v[114:115], v[24:25]
	v_pk_mul_f32 v[116:117], v[116:117], v[24:25]
	v_pk_mul_f32 v[118:119], v[118:119], v[24:25]
	v_pk_mul_f32 v[120:121], v[120:121], v[24:25]
	v_pk_mul_f32 v[122:123], v[122:123], v[24:25]
	v_pk_mul_f32 v[124:125], v[124:125], v[24:25]
	v_pk_mul_f32 v[126:127], v[126:127], v[24:25]
	v_cvt_pk_fp8_f32 v32, v96, v100
	v_cvt_pk_fp8_f32 v33, v112, v116
	v_cvt_pk_fp8_f32 v34, v97, v101
	v_cvt_pk_fp8_f32 v35, v113, v117
	v_cvt_pk_fp8_f32 v36, v98, v102
	v_cvt_pk_fp8_f32 v37, v114, v118
	v_cvt_pk_fp8_f32 v38, v99, v103
	v_cvt_pk_fp8_f32 v39, v115, v119
	v_cvt_pk_fp8_f32 v32, v104, v108 op_sel:[0,0,1]
	v_cvt_pk_fp8_f32 v33, v120, v124 op_sel:[0,0,1]
	v_cvt_pk_fp8_f32 v34, v105, v109 op_sel:[0,0,1]
	v_cvt_pk_fp8_f32 v35, v121, v125 op_sel:[0,0,1]
	v_cvt_pk_fp8_f32 v36, v106, v110 op_sel:[0,0,1]
	v_cvt_pk_fp8_f32 v37, v122, v126 op_sel:[0,0,1]
	v_cvt_pk_fp8_f32 v38, v107, v111 op_sel:[0,0,1]
	v_cvt_pk_fp8_f32 v39, v123, v127 op_sel:[0,0,1]
	s_nop 1
	ds_write_b64 v12, v[32:33]
	ds_write_b64 v12, v[34:35] offset:128
	ds_write_b64 v12, v[36:37] offset:256
	ds_write_b64 v12, v[38:39] offset:384
	s_waitcnt vmcnt(16)
	v_pk_mul_f32 v[128:129], v[128:129], v[24:25]
	v_pk_mul_f32 v[130:131], v[130:131], v[24:25]
	v_pk_mul_f32 v[132:133], v[132:133], v[24:25]
	v_pk_mul_f32 v[134:135], v[134:135], v[24:25]
	v_pk_mul_f32 v[136:137], v[136:137], v[24:25]
	v_pk_mul_f32 v[138:139], v[138:139], v[24:25]
	v_pk_mul_f32 v[140:141], v[140:141], v[24:25]
	v_pk_mul_f32 v[142:143], v[142:143], v[24:25]
	v_pk_mul_f32 v[144:145], v[144:145], v[24:25]
	v_pk_mul_f32 v[146:147], v[146:147], v[24:25]
	v_pk_mul_f32 v[148:149], v[148:149], v[24:25]
	v_pk_mul_f32 v[150:151], v[150:151], v[24:25]
	v_pk_mul_f32 v[152:153], v[152:153], v[24:25]
	v_pk_mul_f32 v[154:155], v[154:155], v[24:25]
	v_pk_mul_f32 v[156:157], v[156:157], v[24:25]
	v_pk_mul_f32 v[158:159], v[158:159], v[24:25]
	v_cvt_pk_fp8_f32 v40, v128, v132
	v_cvt_pk_fp8_f32 v41, v144, v148
	v_cvt_pk_fp8_f32 v42, v129, v133
	v_cvt_pk_fp8_f32 v43, v145, v149
	v_cvt_pk_fp8_f32 v44, v130, v134
	v_cvt_pk_fp8_f32 v45, v146, v150
	v_cvt_pk_fp8_f32 v46, v131, v135
	v_cvt_pk_fp8_f32 v47, v147, v151
	v_cvt_pk_fp8_f32 v40, v136, v140 op_sel:[0,0,1]
	v_cvt_pk_fp8_f32 v41, v152, v156 op_sel:[0,0,1]
	v_cvt_pk_fp8_f32 v42, v137, v141 op_sel:[0,0,1]
	v_cvt_pk_fp8_f32 v43, v153, v157 op_sel:[0,0,1]
	v_cvt_pk_fp8_f32 v44, v138, v142 op_sel:[0,0,1]
	v_cvt_pk_fp8_f32 v45, v154, v158 op_sel:[0,0,1]
	v_cvt_pk_fp8_f32 v46, v139, v143 op_sel:[0,0,1]
	v_cvt_pk_fp8_f32 v47, v155, v159 op_sel:[0,0,1]
	s_nop 1
	ds_write_b64 v13, v[40:41]
	ds_write_b64 v13, v[42:43] offset:128
	ds_write_b64 v13, v[44:45] offset:256
	ds_write_b64 v13, v[46:47] offset:384
	s_waitcnt vmcnt(8)
	v_pk_mul_f32 v[160:161], v[160:161], v[24:25]
	v_pk_mul_f32 v[162:163], v[162:163], v[24:25]
	v_pk_mul_f32 v[164:165], v[164:165], v[24:25]
	v_pk_mul_f32 v[166:167], v[166:167], v[24:25]
	v_pk_mul_f32 v[168:169], v[168:169], v[24:25]
	v_pk_mul_f32 v[170:171], v[170:171], v[24:25]
	v_pk_mul_f32 v[172:173], v[172:173], v[24:25]
	v_pk_mul_f32 v[174:175], v[174:175], v[24:25]
	v_pk_mul_f32 v[176:177], v[176:177], v[24:25]
	v_pk_mul_f32 v[178:179], v[178:179], v[24:25]
	v_pk_mul_f32 v[180:181], v[180:181], v[24:25]
	v_pk_mul_f32 v[182:183], v[182:183], v[24:25]
	v_pk_mul_f32 v[184:185], v[184:185], v[24:25]
	v_pk_mul_f32 v[186:187], v[186:187], v[24:25]
	v_pk_mul_f32 v[188:189], v[188:189], v[24:25]
	v_pk_mul_f32 v[190:191], v[190:191], v[24:25]
	v_cvt_pk_fp8_f32 v32, v160, v164
	v_cvt_pk_fp8_f32 v33, v176, v180
	v_cvt_pk_fp8_f32 v34, v161, v165
	v_cvt_pk_fp8_f32 v35, v177, v181
	v_cvt_pk_fp8_f32 v36, v162, v166
	v_cvt_pk_fp8_f32 v37, v178, v182
	v_cvt_pk_fp8_f32 v38, v163, v167
	v_cvt_pk_fp8_f32 v39, v179, v183
	v_cvt_pk_fp8_f32 v32, v168, v172 op_sel:[0,0,1]
	v_cvt_pk_fp8_f32 v33, v184, v188 op_sel:[0,0,1]
	v_cvt_pk_fp8_f32 v34, v169, v173 op_sel:[0,0,1]
	v_cvt_pk_fp8_f32 v35, v185, v189 op_sel:[0,0,1]
	v_cvt_pk_fp8_f32 v36, v170, v174 op_sel:[0,0,1]
	v_cvt_pk_fp8_f32 v37, v186, v190 op_sel:[0,0,1]
	v_cvt_pk_fp8_f32 v38, v171, v175 op_sel:[0,0,1]
	v_cvt_pk_fp8_f32 v39, v187, v191 op_sel:[0,0,1]
	s_nop 1
	ds_write_b64 v14, v[32:33]
	ds_write_b64 v14, v[34:35] offset:128
	ds_write_b64 v14, v[36:37] offset:256
	ds_write_b64 v14, v[38:39] offset:384
	s_waitcnt vmcnt(0)
	v_pk_mul_f32 v[192:193], v[192:193], v[24:25]
	v_pk_mul_f32 v[194:195], v[194:195], v[24:25]
	v_pk_mul_f32 v[196:197], v[196:197], v[24:25]
	v_pk_mul_f32 v[198:199], v[198:199], v[24:25]
	v_pk_mul_f32 v[200:201], v[200:201], v[24:25]
	v_pk_mul_f32 v[202:203], v[202:203], v[24:25]
	v_pk_mul_f32 v[204:205], v[204:205], v[24:25]
	v_pk_mul_f32 v[206:207], v[206:207], v[24:25]
	v_pk_mul_f32 v[208:209], v[208:209], v[24:25]
	v_pk_mul_f32 v[210:211], v[210:211], v[24:25]
	v_pk_mul_f32 v[212:213], v[212:213], v[24:25]
	v_pk_mul_f32 v[214:215], v[214:215], v[24:25]
	v_pk_mul_f32 v[216:217], v[216:217], v[24:25]
	v_pk_mul_f32 v[218:219], v[218:219], v[24:25]
	v_pk_mul_f32 v[220:221], v[220:221], v[24:25]
	v_pk_mul_f32 v[222:223], v[222:223], v[24:25]
	v_cvt_pk_fp8_f32 v40, v192, v196
	v_cvt_pk_fp8_f32 v41, v208, v212
	v_cvt_pk_fp8_f32 v42, v193, v197
	v_cvt_pk_fp8_f32 v43, v209, v213
	v_cvt_pk_fp8_f32 v44, v194, v198
	v_cvt_pk_fp8_f32 v45, v210, v214
	v_cvt_pk_fp8_f32 v46, v195, v199
	v_cvt_pk_fp8_f32 v47, v211, v215
	v_cvt_pk_fp8_f32 v40, v200, v204 op_sel:[0,0,1]
	v_cvt_pk_fp8_f32 v41, v216, v220 op_sel:[0,0,1]
	v_cvt_pk_fp8_f32 v42, v201, v205 op_sel:[0,0,1]
	v_cvt_pk_fp8_f32 v43, v217, v221 op_sel:[0,0,1]
	v_cvt_pk_fp8_f32 v44, v202, v206 op_sel:[0,0,1]
	v_cvt_pk_fp8_f32 v45, v218, v222 op_sel:[0,0,1]
	v_cvt_pk_fp8_f32 v46, v203, v207 op_sel:[0,0,1]
	v_cvt_pk_fp8_f32 v47, v219, v223 op_sel:[0,0,1]
	s_nop 1
	ds_write_b64 v15, v[40:41]
	ds_write_b64 v15, v[42:43] offset:128
	ds_write_b64 v15, v[44:45] offset:256
	ds_write_b64 v15, v[46:47] offset:384
	s_mov_b64 s[30:31], s[32:33]
	ds_read_b128 v[48:51], v16
	ds_read_b128 v[52:55], v17 offset:1024
	ds_read_b128 v[56:59], v18 offset:2048
	ds_read_b128 v[60:63], v19 offset:3072
	ds_read_b128 v[64:67], v16 offset:4096
	ds_read_b128 v[68:71], v17 offset:5120
	ds_read_b128 v[72:75], v18 offset:6144
	ds_read_b128 v[76:79], v19 offset:7168
	s_waitcnt lgkmcnt(7)
	global_store_dwordx4 v11, v[48:51], s[30:31] nt
	s_add_u32 s30, s30, s24
	s_addc_u32 s31, s31, 0
	s_waitcnt lgkmcnt(6)
	global_store_dwordx4 v11, v[52:55], s[30:31] nt
	s_add_u32 s30, s30, s24
	s_addc_u32 s31, s31, 0
	s_waitcnt lgkmcnt(5)
	global_store_dwordx4 v11, v[56:59], s[30:31] nt
	s_add_u32 s30, s30, s24
	s_addc_u32 s31, s31, 0
	s_waitcnt lgkmcnt(4)
	global_store_dwordx4 v11, v[60:63], s[30:31] nt
	s_add_u32 s30, s30, s24
	s_addc_u32 s31, s31, 0
	s_waitcnt lgkmcnt(3)
	global_store_dwordx4 v11, v[64:67], s[30:31] nt
	s_add_u32 s30, s30, s24
	s_addc_u32 s31, s31, 0
	s_waitcnt lgkmcnt(2)
	global_store_dwordx4 v11, v[68:71], s[30:31] nt
	s_add_u32 s30, s30, s24
	s_addc_u32 s31, s31, 0
	s_waitcnt lgkmcnt(1)
	global_store_dwordx4 v11, v[72:75], s[30:31] nt
	s_add_u32 s30, s30, s24
	s_addc_u32 s31, s31, 0
	s_waitcnt lgkmcnt(0)
	global_store_dwordx4 v11, v[76:79], s[30:31] nt
	s_add_u32 s30, s30, s24
	s_addc_u32 s31, s31, 0
.Lcv_exit:
	s_branch .LBB0_182
.LBB0_182:
	v_readlane_b32 s0, v254, 1
	s_cmp_gt_i32 s0, 1
	s_cselect_b64 s[6:7], -1, 0
	s_and_b64 s[0:1], s[52:53], s[6:7]
	s_andn2_b64 vcc, exec, s[0:1]
	s_cbranch_vccnz .LBB0_227
	s_waitcnt vmcnt(0)
	s_barrier
	s_mov_b64 s[8:9], exec
	v_readlane_b32 s0, v254, 4
	v_readlane_b32 s1, v254, 5
	s_and_b64 s[0:1], s[8:9], s[0:1]
	s_mov_b64 exec, s[0:1]
	s_cbranch_execz .LBB0_226
	v_readlane_b32 s0, v254, 6
	s_waitcnt vmcnt(0) expcnt(0) lgkmcnt(0)
	s_nop 0
	v_mov_b32_e32 v1, s0
	ds_read_b32 v3, v1
	ds_read_b32 v1, v1 offset:4
	s_waitcnt lgkmcnt(1)
	v_cmp_ne_u32_e32 vcc, 0, v3
	s_cbranch_vccnz .LBB0_197
	v_readlane_b32 s2, v254, 2
	v_readlane_b32 s3, v254, 3
	s_add_u32 s10, s76, 0x1000
	s_load_dwordx2 s[0:1], s[2:3], 0x4
	s_addc_u32 s11, s77, 0
	s_add_u32 s12, s76, 0x1100
	s_addc_u32 s13, s77, 0
	s_add_u32 s14, s76, 0x1200
	s_addc_u32 s15, s77, 0
	s_waitcnt lgkmcnt(0)
	s_mul_i32 s0, s0, s74
	s_add_u32 s16, s76, 0x1300
	s_mul_i32 s0, s0, s1
	s_addc_u32 s17, s77, 0
	s_mov_b32 s1, 1
	v_mov_b32_e32 v17, 0
	s_branch .LBB0_187
